# S2 + XCD-contiguous block->tile remap in attn kernel (B-fragment L2 locality)
# baseline (speedup 1.0000x reference)
_Z11attn_kernelPKiPKDv8_DF16_PKDF16_S5_PDF16_Pf:
	s_and_b32 s3, s2, 7
	s_lshl_b32 s3, s3, 5
	s_lshr_b32 s2, s2, 3
	s_or_b32 s2, s2, s3
	s_mul_i32 s3, s2, 27
	s_mul_hi_i32 s26, s3, 0x2aaaaaab
	v_and_b32_e32 v102, 63, v0
	s_lshr_b32 s27, s26, 31
	s_ashr_i32 s28, s26, 3
	s_movk_i32 s4, 0x200
	v_lshrrev_b32_e32 v98, 6, v0
	s_add_i32 s28, s28, s27
	v_cmp_gt_u32_e32 vcc, s4, v0
	s_mul_hi_i32 s29, s3, 0x38e38e39
	v_lshlrev_b32_e32 v122, 4, v102
	s_and_saveexec_b64 s[4:5], vcc
	s_xor_b64 s[12:13], exec, s[4:5]
	s_cbranch_execz .LBB1_65
	s_lshr_b32 s6, s29, 31
	s_ashr_i32 s7, s29, 9
	s_add_i32 s6, s7, s6
	s_mul_i32 s7, s6, 0xffffffd0
	v_bfe_u32 v117, v0, 6, 2
	s_add_i32 s7, s7, s28
	v_lshl_or_b32 v4, s6, 2, v117
	s_lshl_b32 s6, s7, 6
	s_load_dwordx2 s[4:5], s[0:1], 0x8
	s_load_dwordx4 s[8:11], s[0:1], 0x18
	s_load_dwordx2 s[14:15], s[0:1], 0x28
	s_movk_i32 s30, 0xc00
	v_mov_b32_e32 v2, s6
	v_and_b32_e32 v119, 31, v0
	v_mad_i32_i24 v2, v4, s30, v2
	v_or_b32_e32 v2, v2, v119
	s_mul_i32 s6, s28, 48
	v_ashrrev_i32_e32 v3, 31, v2
	s_sub_i32 s6, s3, s6
	s_waitcnt lgkmcnt(0)
	v_lshl_add_u64 v[2:3], v[2:3], 1, s[8:9]
	s_lshl_b32 s6, s6, 2
	global_load_ushort v5, v[2:3], off
	global_load_ushort v6, v[2:3], off offset:64
	s_movk_i32 s31, 0xc0
	v_mov_b32_e32 v2, s6
	s_add_i32 s6, s3, 1
	v_mad_i32_i24 v2, v4, s31, v2
	v_lshrrev_b32_e32 v4, 7, v0
	s_mul_hi_i32 s7, s6, 0x2aaaaaab
	v_and_b32_e32 v121, 2, v4
	s_lshr_b32 s16, s7, 31
	s_lshr_b32 s7, s7, 3
	v_or_b32_e32 v2, v2, v121
	s_add_i32 s7, s7, s16
	v_ashrrev_i32_e32 v3, 31, v2
	s_mul_i32 s7, s7, 48
	v_lshlrev_b64 v[2:3], 11, v[2:3]
	s_sub_i32 s7, s6, s7
	s_mul_hi_i32 s6, s6, 0x38e38e39
	v_lshl_add_u64 v[2:3], s[4:5], 0, v[2:3]
	v_mov_b32_e32 v123, 0
	s_lshr_b32 s16, s6, 31
	s_lshr_b32 s6, s6, 9
	v_lshl_add_u64 v[2:3], v[2:3], 0, v[122:123]
	s_add_i32 s6, s6, s16
	global_load_dwordx4 v[86:89], v[2:3], off
	global_load_dwordx4 v[82:85], v[2:3], off offset:1024
	global_load_dwordx4 v[70:73], v[2:3], off offset:2048
	global_load_dwordx4 v[66:69], v[2:3], off offset:3072
	v_lshl_or_b32 v2, s6, 2, v117
	s_lshl_b32 s6, s7, 2
	v_mov_b32_e32 v3, s6
	v_mad_i32_i24 v2, v2, s31, v3
	v_or_b32_e32 v2, v2, v121
	v_ashrrev_i32_e32 v3, 31, v2
	v_lshlrev_b64 v[2:3], 11, v[2:3]
	v_lshl_add_u64 v[2:3], s[4:5], 0, v[2:3]
	v_lshl_add_u64 v[2:3], v[2:3], 0, v[122:123]
	global_load_dwordx4 v[94:97], v[2:3], off
	global_load_dwordx4 v[90:93], v[2:3], off offset:1024
	global_load_dwordx4 v[78:81], v[2:3], off offset:2048
	global_load_dwordx4 v[74:77], v[2:3], off offset:3072
	v_lshlrev_b32_e32 v3, 2, v102
	v_lshrrev_b32_e32 v1, 5, v102
	v_lshl_add_u64 v[114:115], s[4:5], 0, v[122:123]
	s_movk_i32 s4, 0xff
	v_lshl_or_b32 v127, v117, 14, v3
	v_lshlrev_b32_e32 v3, 8, v117
	v_lshlrev_b32_e32 v7, 2, v119
	s_mov_b32 s16, 0x15000
	v_cmp_lt_u32_e64 s[6:7], s4, v0
	v_or3_b32 v128, v3, v7, s16
	v_lshlrev_b32_e32 v3, 10, v1
	v_and_b32_e32 v0, 0xc0, v0
	v_lshlrev_b32_e32 v2, 1, v117
	v_or3_b32 v124, v3, v0, v119
	v_lshlrev_b32_e32 v0, 3, v121
	v_or3_b32 v0, v2, v0, v1
	v_lshlrev_b32_e32 v8, 6, v117
	v_lshlrev_b32_e32 v129, 5, v0
	v_or_b32_e32 v0, 1, v4
	v_or3_b32 v116, v3, v8, v119
	v_lshlrev_b32_e32 v3, 3, v0
	v_lshlrev_b32_e32 v125, 4, v1
	s_movk_i32 s16, 0x80
	v_or3_b32 v1, v2, v3, v1
	v_lshlrev_b32_e32 v133, 5, v0
	s_mov_b32 s36, 0x5040100
	v_mbcnt_lo_u32_b32 v0, -1, 0
	s_add_i32 s33, s3, 2
	v_cmp_gt_u32_e64 s[4:5], 32, v102
	s_lshl_b32 s34, s2, 1
	s_movk_i32 s35, 0x2000
	v_or_b32_e32 v118, 0x2000, v116
	v_or3_b32 v120, v7, v117, s16
	v_add_u32_e32 v126, v7, v98
	v_lshlrev_b32_e32 v130, 5, v121
	v_mul_u32_u24_e32 v131, 0x90, v119
	v_lshlrev_b32_e32 v132, 5, v1
	s_mov_b32 s42, 0
	s_movk_i32 s37, 0x5000
	s_movk_i32 s38, 0x6000
	s_movk_i32 s39, 0x7000
	s_movk_i32 s40, 0x1000
	s_movk_i32 s41, 0x3000
	v_mbcnt_hi_u32_b32 v134, -1, v0
	v_mov_b32_e32 v1, 0
	s_waitcnt vmcnt(9)
	v_perm_b32 v136, v5, v5, s36
	s_waitcnt vmcnt(8)
	v_perm_b32 v135, v6, v6, s36
	v_mov_b32_e32 v122, 0
	v_mov_b32_e32 v18, v123
	v_mov_b32_e32 v19, v123
	v_mov_b32_e32 v20, v123
	v_mov_b32_e32 v21, v123
	v_mov_b32_e32 v22, v123
	v_mov_b32_e32 v23, v123
	v_mov_b32_e32 v24, v123
	v_mov_b32_e32 v25, v123
	v_mov_b32_e32 v26, v123
	v_mov_b32_e32 v27, v123
	v_mov_b32_e32 v28, v123
	v_mov_b32_e32 v29, v123
	v_mov_b32_e32 v30, v123
	v_mov_b32_e32 v31, v123
	v_mov_b32_e32 v32, v123
	v_mov_b32_e32 v33, v123
	v_mov_b32_e32 v50, v123
	v_mov_b32_e32 v51, v123
	v_mov_b32_e32 v52, v123
	v_mov_b32_e32 v53, v123
	v_mov_b32_e32 v54, v123
	v_mov_b32_e32 v55, v123
	v_mov_b32_e32 v56, v123
	v_mov_b32_e32 v57, v123
	v_mov_b32_e32 v58, v123
	v_mov_b32_e32 v59, v123
	v_mov_b32_e32 v60, v123
	v_mov_b32_e32 v61, v123
	v_mov_b32_e32 v62, v123
	v_mov_b32_e32 v63, v123
	v_mov_b32_e32 v64, v123
	v_mov_b32_e32 v65, v123
	v_mov_b32_e32 v2, v123
	v_mov_b32_e32 v3, v123
	v_mov_b32_e32 v4, v123
	v_mov_b32_e32 v5, v123
	v_mov_b32_e32 v6, v123
	v_mov_b32_e32 v7, v123
	v_mov_b32_e32 v8, v123
	v_mov_b32_e32 v9, v123
	v_mov_b32_e32 v10, v123
	v_mov_b32_e32 v11, v123
	v_mov_b32_e32 v12, v123
	v_mov_b32_e32 v13, v123
	v_mov_b32_e32 v14, v123
	v_mov_b32_e32 v15, v123
	v_mov_b32_e32 v16, v123
	v_mov_b32_e32 v17, v123
	v_mov_b32_e32 v34, v123
	v_mov_b32_e32 v35, v123
	v_mov_b32_e32 v36, v123
	v_mov_b32_e32 v37, v123
	v_mov_b32_e32 v38, v123
	v_mov_b32_e32 v39, v123
	v_mov_b32_e32 v40, v123
	v_mov_b32_e32 v41, v123
	v_mov_b32_e32 v42, v123
	v_mov_b32_e32 v43, v123
	v_mov_b32_e32 v44, v123
	v_mov_b32_e32 v45, v123
	v_mov_b32_e32 v46, v123
	v_mov_b32_e32 v47, v123
	v_mov_b32_e32 v48, v123
	v_mov_b32_e32 v49, v123
	v_add3_u32 v137, v125, v130, v131
	v_lshlrev_b32_e32 v118, 4, v134
	v_readfirstlane_b32 s52, v114
	v_readfirstlane_b32 s53, v115
	v_readfirstlane_b32 s57, v117
	v_readfirstlane_b32 s58, v121
	v_bfe_u32 v138, v134, 4, 1
	v_bfe_u32 v139, v134, 3, 1
	v_cmp_eq_u32_e32 vcc, v138, v139
	v_mov_b32_e32 v155, 0x3c003c00
	s_nop 1
	v_cndmask_b32_e32 v154, 0, v155, vcc
	v_mov_b32_e32 v122, 0
	v_mov_b32_e32 v155, v154
	v_mov_b32_e32 v156, v154
	v_mov_b32_e32 v157, v154
	v_mov_b32_e32 v123, 0
	v_mov_b32_e32 v124, 0
	v_mov_b32_e32 v125, 0
	v_mov_b32_e32 v146, 0
	v_mov_b32_e32 v147, 0
	v_mov_b32_e32 v148, 0
	v_mov_b32_e32 v149, 0
	s_mov_b32 s49, s28
	s_mul_i32 s50, s28, 48
	s_sub_i32 s50, s3, s50
	s_add_i32 s50, s50, -1
	s_mov_b32 s55, 0
	s_mov_b32 s56, 0
	s_mul_hi_u32 s59, s33, 0x2aaaaaab
	s_lshr_b32 s59, s59, 3
	s_mul_i32 s60, s59, 48
	s_sub_i32 s51, s33, s60
	s_mul_hi_u32 s60, s59, 0x2aaaaaab
	s_lshr_b32 s60, s60, 3
	s_mul_i32 s54, s60, 48
	s_sub_i32 s54, s59, s54
	s_lshl_b32 s60, s60, 2
	s_add_i32 s60, s60, s57
	s_mul_i32 s60, s60, 0xc0
	s_lshl_b32 s59, s51, 2
	s_add_i32 s60, s60, s59
	s_add_i32 s60, s60, s58
	s_lshl_b32 s60, s60, 11
	s_add_u32 s52, s52, s60
	s_addc_u32 s53, s53, 0
	s_barrier
	s_branch .LBB1_4
